# v11: v10 + the next chunk's ready flag is read one chunk ahead in the scan state waves
# baseline (speedup 1.0000x reference)
.LBB0_1732:
	s_lshl_b32 s0, s69, 2
	s_add_i32 s76, s0, 0
	s_add_i32 s76, s76, 0x27a00
	s_cmp_eq_u32 s69, 0
	s_cbranch_scc1 .Lx_fl_read
	s_waitcnt lgkmcnt(0)
	v_cmp_lt_i32_e32 vcc, s71, v214
	s_cbranch_vccnz .LBB0_1734
	s_branch .LBB0_1733
.Lx_fl_read:
	v_mov_b32_e32 v18, s76
	ds_read_b32 v18, v18
	s_waitcnt lgkmcnt(0)
	v_cmp_lt_i32_e32 vcc, s71, v18
	s_cbranch_vccnz .LBB0_1734

.LBB0_1734:
	v_mov_b32_e32 v215, s76
	ds_read_b32 v214, v215 offset:4
	s_mul_i32 s0, s69, 0x3300
	s_add_i32 s0, s74, s0
	s_add_i32 s1, s0, 0x2a00
	v_add_u32_e32 v18, s1, v185
	ds_read_b64_tr_b16 v[20:21], v18
	v_add3_u32 v18, s0, v186, v187
	ds_read2_b64 v[26:29], v18 offset1:4
	ds_read2_b64 v[30:33], v18 offset0:8 offset1:12
	v_add_u32_e32 v18, 0x800, v18
	v_cvt_pk_bf16_f32 v22, v2, v3
	v_cvt_pk_bf16_f32 v23, v4, v5
	v_cvt_pk_bf16_f32 v24, v10, v11
	v_cvt_pk_bf16_f32 v25, v12, v13
	ds_read2_b64 v[38:41], v18 offset0:32 offset1:36
	ds_read2_b64 v[42:45], v18 offset0:40 offset1:44
	s_waitcnt lgkmcnt(3)
	v_mfma_f32_16x16x32_bf16 v[26:29], v[26:29], v[22:25], 0
	s_waitcnt lgkmcnt(0)
	s_add_i32 s76, s69, s68
	v_cvt_pk_bf16_f32 v34, v6, v7
	v_cvt_pk_bf16_f32 v35, v8, v9
	v_cvt_pk_bf16_f32 v36, v14, v15
	v_cvt_pk_bf16_f32 v37, v16, v17
	s_waitcnt lgkmcnt(2)
	s_nop 0
	v_mfma_f32_16x16x32_bf16 v[26:29], v[30:33], v[34:37], v[26:29]
	s_nop 7
	v_cvt_pk_bf16_f32 v18, v26, v27
	v_add_u32_e32 v26, s0, v192
	ds_read_b128 v[30:33], v26 offset:8704
	v_add_u32_e32 v62, s0, v191
	ds_read_b128 v[46:49], v62 offset:12800
	v_cvt_pk_bf16_f32 v19, v28, v29
	ds_read_b128 v[26:29], v26 offset:9728
	ds_read_b128 v[50:53], v62 offset:12864
	v_add_u32_e32 v63, v62, v190
	ds_read_b128 v[54:57], v63 offset:4608
	ds_read_b128 v[58:61], v63 offset:5632
	s_waitcnt lgkmcnt(5)
	v_mfma_f32_16x16x32_bf16 v[30:33], v[30:33], v[18:21], 0
	s_waitcnt lgkmcnt(2)
	v_pk_mul_f32 v[10:11], v[10:11], v[50:51]
	v_pk_mul_f32 v[12:13], v[12:13], v[52:53]
	ds_read_b128 v[50:53], v63 offset:7680
	v_mfma_f32_16x16x32_bf16 v[22:25], v[38:41], v[22:25], 0
	s_nop 2
	v_cvt_pk_bf16_f32 v18, v30, v31
	v_cvt_pk_bf16_f32 v19, v32, v33
	ds_read_b128 v[30:33], v63 offset:6656
	v_pk_mul_f32 v[2:3], v[2:3], v[46:47]
	v_pk_mul_f32 v[4:5], v[4:5], v[48:49]
	ds_read_b128 v[46:49], v62 offset:12928
	v_mfma_f32_16x16x32_bf16 v[22:25], v[42:45], v[34:37], v[22:25]
	s_cmp_lt_u32 s76, 16
	s_waitcnt lgkmcnt(4)
	v_mfma_f32_16x16x32_bf16 v[2:5], v[54:57], v[18:21], v[2:5]
	ds_read_b128 v[54:57], v62 offset:12992
	s_waitcnt lgkmcnt(1)
	v_pk_mul_f32 v[6:7], v[6:7], v[46:47]
	v_pk_mul_f32 v[8:9], v[8:9], v[48:49]
	v_mfma_f32_16x16x32_bf16 v[10:13], v[58:61], v[18:21], v[10:13]
	s_waitcnt lgkmcnt(0)
	v_pk_mul_f32 v[14:15], v[14:15], v[54:55]
	v_pk_mul_f32 v[16:17], v[16:17], v[56:57]
	v_mfma_f32_16x16x32_bf16 v[6:9], v[30:33], v[18:21], v[6:9]
	s_nop 0
	v_mfma_f32_16x16x32_bf16 v[14:17], v[50:53], v[18:21], v[14:17]
	v_mfma_f32_16x16x32_bf16 v[18:21], v[26:29], v[18:21], v[22:25]
	s_cbranch_scc1 .LBB0_1731
	s_nop 6
	v_mov_b32_dpp v32, v18 quad_perm:[1,0,3,2] row_mask:0xf bank_mask:0xf bound_ctrl:1
	v_mov_b32_dpp v33, v19 quad_perm:[1,0,3,2] row_mask:0xf bank_mask:0xf bound_ctrl:1
	v_mov_b32_dpp v34, v20 quad_perm:[1,0,3,2] row_mask:0xf bank_mask:0xf bound_ctrl:1
	v_mov_b32_dpp v35, v21 quad_perm:[1,0,3,2] row_mask:0xf bank_mask:0xf bound_ctrl:1
	v_cndmask_b32_e64 v36, v18, v33, s[98:99]
	v_cndmask_b32_e64 v37, v32, v19, s[98:99]
	v_cndmask_b32_e64 v38, v20, v35, s[98:99]
	v_cndmask_b32_e64 v39, v34, v21, s[98:99]
	v_cvt_pk_bf16_f32 v36, v36, v37
	v_cvt_pk_bf16_f32 v38, v38, v39
	global_store_dword v[210:211], v36, off sc1
	global_store_dword v[212:213], v38, off sc1
	s_branch .LBB0_1731
